# norm row loops (layers 1-3): next row's loads now overlap the current row's math (single counted wait before the register hand-over)
# baseline (speedup 1.0000x reference)
; #define LOADROW(R, m) do { if (l == 0) load_rowraw(R, SRC(m), nullptr, F.lane); else load_rowraw_b(R, X + (size_t)(m) * 1024, Y + (size_t)(m) * 2048, F.lane); } while (0)
; __device__ __forceinline__ void unpack_x(RowRaw& R) {
; #pragma unroll
;     for (int j = 0; j < 4; ++j) { const u32x2 t = R.xb[j]; R.x[j] = (f32x4){bf16lo(t.x), bf16hi(t.x), bf16lo(t.y), bf16hi(t.y)}; }
; }
; __device__ __forceinline__ void combine_raw(RowRaw& R, const RowVec& V) {
; #pragma unroll
;     for (int j = 0; j < 4; ++j) { const u32x2 a = R.y0[j], b = R.y1[j];
;         R.x[j].x += V.g[j].x * (bf16lo(a.x) + bf16lo(b.x)); R.x[j].y += V.g[j].y * (bf16hi(a.x) + bf16hi(b.x));
;         R.x[j].z += V.g[j].z * (bf16lo(a.y) + bf16lo(b.y)); R.x[j].w += V.g[j].w * (bf16hi(a.y) + bf16hi(b.y)); }
; }
; __device__ __forceinline__ void mix_norm_phase(Frame& F, int l) {
;     ...
;     for (int m = r0; m < r1; ++m) {
;         cur = nxt;
;         if (m + 1 < r1) LOADROW(nxt, m + 1);
;         const int v = row_class(m);
;         if (v != vcur) { vcur = v; const float* mv = mod + (size_t)(l * 3 + v) * 6144;
;             load_rowvec(V, gain, mv, mv + 1024, l > 0 ? mod + ((size_t)((l - 1) * 3 + v) * 6 + 5) * 1024 : nullptr, F.lane); }
;         if (l > 0) {
;             unpack_x(cur); combine_raw(cur, V);
;             store_bf16_row(X + (size_t)m * 1024, F.lane, cur.x); }
;         const float rs = row_rs(cur.x);
;         f32x4 h[4];
; #pragma unroll
;         for (int j = 0; j < 4; ++j) h[j] = (cur.x[j] * rs) * V.a[j] + V.b[j];
;         store_bf16_row(H + (size_t)m * 1024, F.lane, h);
.LBB0_1779:
	v_lshlrev_b32_e32 v116, 16, v104
	v_and_b32_e32 v117, 0xffff0000, v104
	v_lshlrev_b32_e32 v118, 16, v106
	v_and_b32_e32 v119, 0xffff0000, v106
	v_lshlrev_b32_e32 v104, 16, v105
	v_and_b32_e32 v105, 0xffff0000, v105
	v_lshlrev_b32_e32 v106, 16, v107
	v_and_b32_e32 v107, 0xffff0000, v107
	v_lshlrev_b32_e32 v114, 16, v108
	v_and_b32_e32 v115, 0xffff0000, v108
	v_pk_add_f32 v[116:117], v[116:117], v[118:119]
	v_lshlrev_b32_e32 v108, 16, v109
	v_and_b32_e32 v109, 0xffff0000, v109
	v_pk_add_f32 v[104:105], v[104:105], v[106:107]
	v_pk_fma_f32 v[114:115], v[116:117], v[14:15], v[114:115]
	v_pk_fma_f32 v[104:105], v[104:105], v[16:17], v[108:109]
	v_lshlrev_b32_e32 v108, 16, v102
	v_and_b32_e32 v109, 0xffff0000, v102
	v_lshlrev_b32_e32 v116, 16, v100
	v_and_b32_e32 v117, 0xffff0000, v100
	v_lshlrev_b32_e32 v106, 16, v98
	v_and_b32_e32 v107, 0xffff0000, v98
	v_pk_add_f32 v[108:109], v[108:109], v[116:117]
	v_lshlrev_b32_e32 v102, 16, v103
	v_and_b32_e32 v103, 0xffff0000, v103
	v_lshlrev_b32_e32 v100, 16, v101
	v_and_b32_e32 v101, 0xffff0000, v101
	v_pk_fma_f32 v[106:107], v[108:109], v[18:19], v[106:107]
	v_lshlrev_b32_e32 v98, 16, v99
	v_and_b32_e32 v99, 0xffff0000, v99
	v_pk_add_f32 v[100:101], v[102:103], v[100:101]
	v_lshlrev_b32_e32 v102, 16, v96
	v_and_b32_e32 v103, 0xffff0000, v96
	v_lshlrev_b32_e32 v108, 16, v92
	v_and_b32_e32 v109, 0xffff0000, v92
	v_pk_fma_f32 v[98:99], v[100:101], v[20:21], v[98:99]
	v_lshlrev_b32_e32 v100, 16, v90
	v_and_b32_e32 v101, 0xffff0000, v90
	v_pk_add_f32 v[102:103], v[102:103], v[108:109]
	v_lshlrev_b32_e32 v96, 16, v97
	v_and_b32_e32 v97, 0xffff0000, v97
	v_lshlrev_b32_e32 v92, 16, v93
	v_and_b32_e32 v93, 0xffff0000, v93
	v_pk_fma_f32 v[100:101], v[102:103], v[22:23], v[100:101]
	v_lshlrev_b32_e32 v90, 16, v91
	v_and_b32_e32 v91, 0xffff0000, v91
	v_pk_add_f32 v[92:93], v[96:97], v[92:93]
	v_lshlrev_b32_e32 v96, 16, v88
	v_and_b32_e32 v97, 0xffff0000, v88
	v_lshlrev_b32_e32 v102, 16, v86
	v_and_b32_e32 v103, 0xffff0000, v86
	v_lshlrev_b32_e32 v88, 16, v89
	v_and_b32_e32 v89, 0xffff0000, v89
	v_lshlrev_b32_e32 v86, 16, v87
	v_and_b32_e32 v87, 0xffff0000, v87
	v_pk_fma_f32 v[90:91], v[92:93], v[24:25], v[90:91]
	v_lshlrev_b32_e32 v92, 16, v84
	v_and_b32_e32 v93, 0xffff0000, v84
	v_lshlrev_b32_e32 v84, 16, v85
	v_and_b32_e32 v85, 0xffff0000, v85
	v_pk_add_f32 v[86:87], v[88:89], v[86:87]
	v_add_co_u32_e32 v88, vcc, s11, v94
	v_pk_fma_f32 v[84:85], v[86:87], v[40:41], v[84:85]
	v_cvt_pk_bf16_f32 v86, v114, v115
	v_cvt_pk_bf16_f32 v87, v104, v105
	v_addc_co_u32_e32 v89, vcc, 0, v95, vcc
	global_store_dwordx2 v[88:89], v[86:87], off
	v_cvt_pk_bf16_f32 v86, v106, v107
	v_cvt_pk_bf16_f32 v87, v98, v99
	v_pk_add_f32 v[96:97], v[96:97], v[102:103]
	global_store_dwordx2 v[88:89], v[86:87], off offset:512
	v_cvt_pk_bf16_f32 v86, v100, v101
	v_cvt_pk_bf16_f32 v87, v90, v91
	v_pk_fma_f32 v[92:93], v[96:97], v[38:39], v[92:93]
	global_store_dwordx2 v[88:89], v[86:87], off offset:1024
	v_pk_mul_f32 v[86:87], v[114:115], v[114:115]
	v_pk_mul_f32 v[96:97], v[104:105], v[104:105]
	v_pk_mul_f32 v[102:103], v[106:107], v[106:107]
	v_pk_mul_f32 v[108:109], v[98:99], v[98:99]
	v_add_f32_e32 v96, v96, v97
	v_add_f32_e32 v86, v86, v87
	v_add_f32_e32 v86, v86, v96
	v_add_f32_e32 v87, v108, v109
	v_add_f32_e32 v96, v102, v103
	v_pk_mul_f32 v[116:117], v[100:101], v[100:101]
	v_pk_mul_f32 v[118:119], v[90:91], v[90:91]
	v_add_f32_e32 v87, v96, v87
	v_add_f32_e32 v86, v87, v86
	v_add_f32_e32 v87, v118, v119
	v_add_f32_e32 v96, v116, v117
	v_pk_mul_f32 v[120:121], v[92:93], v[92:93]
	v_pk_mul_f32 v[122:123], v[84:85], v[84:85]
	v_add_f32_e32 v87, v96, v87
	v_add_f32_e32 v86, v87, v86
	v_add_f32_e32 v87, v122, v123
	v_add_f32_e32 v96, v120, v121
	v_add_f32_e32 v87, v96, v87
	v_add_f32_e32 v86, v87, v86
	s_add_u32 s2, s2, 0x800
	s_addc_u32 s3, s3, 0
	v_add_f32_dpp v86, v86, v86 quad_perm:[1,0,3,2] row_mask:0xf bank_mask:0xf bound_ctrl:1
	s_add_u32 s4, s4, 0x1000
	s_addc_u32 s5, s5, 0
	v_add_f32_dpp v86, v86, v86 quad_perm:[2,3,0,1] row_mask:0xf bank_mask:0xf bound_ctrl:1
	s_mov_b32 s6, s7
	v_add_f32_dpp v86, v86, v86 row_half_mirror row_mask:0xf bank_mask:0xf bound_ctrl:1
	s_nop 1
	v_add_f32_dpp v86, v86, v86 row_mirror row_mask:0xf bank_mask:0xf bound_ctrl:1
	v_mov_b32_e32 v87, v86
	s_nop 1
	v_permlane16_swap_b32_e32 v86, v87
	v_add_f32_e32 v86, v86, v87
	v_mov_b32_e32 v87, v86
	s_nop 1
	v_permlane32_swap_b32_e32 v86, v87
	v_add_f32_e32 v86, v86, v87
	v_fmamk_f32 v86, v86, 0x3a800000, v1
	v_mul_f32_e32 v87, 0x4b800000, v86
	v_cmp_gt_f32_e32 vcc, s12, v86
	s_nop 1
	v_cndmask_b32_e32 v86, v86, v87, vcc
	v_rsq_f32_e32 v96, v86
	v_cvt_pk_bf16_f32 v86, v92, v93
	v_cvt_pk_bf16_f32 v87, v84, v85
	global_store_dwordx2 v[88:89], v[86:87], off offset:1536
	v_mul_f32_e32 v86, 0x45800000, v96
	v_cndmask_b32_e32 v86, v96, v86, vcc
	v_pk_mul_f32 v[88:89], v[114:115], v[86:87] op_sel_hi:[1,0]
	v_pk_mul_f32 v[92:93], v[92:93], v[86:87] op_sel_hi:[1,0]
	v_pk_mul_f32 v[96:97], v[104:105], v[86:87] op_sel_hi:[1,0]
	v_pk_fma_f32 v[88:89], v[30:31], v[88:89], v[2:3]
	v_pk_mul_f32 v[102:103], v[106:107], v[86:87] op_sel_hi:[1,0]
	v_pk_mul_f32 v[98:99], v[98:99], v[86:87] op_sel_hi:[1,0]
	v_pk_mul_f32 v[100:101], v[100:101], v[86:87] op_sel_hi:[1,0]
	v_pk_mul_f32 v[90:91], v[90:91], v[86:87] op_sel_hi:[1,0]
	v_pk_mul_f32 v[84:85], v[84:85], v[86:87] op_sel_hi:[1,0]
	v_pk_fma_f32 v[86:87], v[46:47], v[92:93], v[26:27]
	v_add_co_u32_e32 v92, vcc, s13, v94
	v_pk_fma_f32 v[96:97], v[32:33], v[96:97], v[4:5]
	v_cvt_pk_bf16_f32 v88, v88, v89
	s_nop 0
	v_addc_co_u32_e32 v93, vcc, 0, v95, vcc
	v_cvt_pk_bf16_f32 v89, v96, v97
	v_pk_fma_f32 v[98:99], v[36:37], v[98:99], v[12:13]
	v_pk_fma_f32 v[102:103], v[34:35], v[102:103], v[10:11]
	global_store_dwordx2 v[92:93], v[88:89], off
	v_cvt_pk_bf16_f32 v88, v102, v103
	v_cvt_pk_bf16_f32 v89, v98, v99
	v_pk_fma_f32 v[90:91], v[44:45], v[90:91], v[8:9]
	v_pk_fma_f32 v[100:101], v[42:43], v[100:101], v[6:7]
	v_pk_fma_f32 v[84:85], v[48:49], v[84:85], v[28:29]
	global_store_dwordx2 v[92:93], v[88:89], off offset:512
	v_cvt_pk_bf16_f32 v88, v100, v101
	v_cvt_pk_bf16_f32 v89, v90, v91
	global_store_dwordx2 v[92:93], v[88:89], off offset:1024
	v_cvt_pk_bf16_f32 v86, v86, v87
	v_cvt_pk_bf16_f32 v87, v84, v85
	global_store_dwordx2 v[92:93], v[86:87], off offset:1536
	s_andn2_b64 vcc, exec, s[8:9]
	s_waitcnt vmcnt(8)
	v_mov_b64_e32 v[108:109], v[66:67]
	v_mov_b64_e32 v[98:99], v[64:65]
	v_mov_b64_e32 v[90:91], v[62:63]
	v_mov_b64_e32 v[84:85], v[60:61]
	v_mov_b64_e32 v[104:105], v[68:69]
	v_mov_b64_e32 v[102:103], v[70:71]
	v_mov_b64_e32 v[96:97], v[72:73]
	v_mov_b64_e32 v[88:89], v[82:83]
	v_mov_b64_e32 v[106:107], v[80:81]
	v_mov_b64_e32 v[100:101], v[78:79]
	v_mov_b64_e32 v[92:93], v[76:77]
	v_mov_b64_e32 v[86:87], v[74:75]
	s_cbranch_vccz .LBB0_1784

; __device__ __forceinline__ void load_rowvec(RowVec& V, const float* gain, const float* sh, const float* sc, const float* g2, int lane) {
; #pragma unroll
;     for (int j = 0; j < 4; ++j) { const int c = 256 * j + 4 * lane;
;         const f32x4 g = *(const f32x4*)(gain + c), s1 = *(const f32x4*)(sc + c); V.a[j] = g * (s1 + 1.f); V.b[j] = *(const f32x4*)(sh + c);
;         V.g[j] = g2 ? *(const f32x4*)(g2 + c) * MOE_ALPHA : (f32x4){0.f, 0.f, 0.f, 0.f}; }
; }
; __device__ __forceinline__ void mix_norm_phase(Frame& F, int l) {
;     ...
;         const int v = row_class(m);
;         if (v != vcur) { vcur = v; const float* mv = mod + (size_t)(l * 3 + v) * 6144;
;             load_rowvec(V, gain, mv, mv + 1024, l > 0 ? mod + ((size_t)((l - 1) * 3 + v) * 6 + 5) * 1024 : nullptr, F.lane); }
.LBB0_1782:
	s_cmpk_lt_u32 s6, 0x8000
	s_cselect_b32 s15, 1, 2
	s_cmpk_gt_i32 s6, 0x3fff
	s_cselect_b32 s6, s15, 0
	s_cmp_eq_u32 s6, s14
	s_cbranch_scc1 .LBB0_1779
	s_mul_i32 s14, s6, 0x6000
	s_add_u32 s18, s1, s14
	s_addc_u32 s19, s10, 0
	s_add_u32 s14, s18, 0x12000
	s_addc_u32 s15, s19, 0
	s_add_u32 s16, s18, 0x13000
	s_addc_u32 s17, s19, 0
	global_load_dwordx4 v[30:33], v110, s[16:17]
	global_load_dwordx4 v[34:37], v111, s[16:17]
	global_load_dwordx4 v[42:45], v[52:53], off
	global_load_dwordx4 v[46:49], v[54:55], off
	global_load_dwordx4 v[114:117], v112, s[16:17]
	global_load_dwordx4 v[118:121], v113, s[16:17]
	global_load_dwordx4 v[122:125], v[56:57], off
	global_load_dwordx4 v[126:129], v[58:59], off
	s_add_u32 s16, s18, 0x5000
	s_addc_u32 s17, s19, 0
	global_load_dwordx4 v[2:5], v110, s[14:15]
	global_load_dwordx4 v[6:9], v112, s[14:15]
	global_load_dwordx4 v[14:17], v110, s[16:17]
	global_load_dwordx4 v[10:13], v111, s[14:15]
	global_load_dwordx4 v[18:21], v111, s[16:17]
	global_load_dwordx4 v[22:25], v112, s[16:17]
	global_load_dwordx4 v[26:29], v113, s[14:15]
	global_load_dwordx4 v[38:41], v113, s[16:17]
	s_mov_b32 s14, s6
	s_waitcnt vmcnt(15)
	v_pk_add_f32 v[32:33], v[32:33], 1.0 op_sel_hi:[1,0]
	v_pk_add_f32 v[30:31], v[30:31], 1.0 op_sel_hi:[1,0]
	s_waitcnt vmcnt(14)
	v_pk_add_f32 v[36:37], v[36:37], 1.0 op_sel_hi:[1,0]
	v_pk_add_f32 v[34:35], v[34:35], 1.0 op_sel_hi:[1,0]
	s_waitcnt vmcnt(11)
	v_pk_add_f32 v[116:117], v[116:117], 1.0 op_sel_hi:[1,0]
	v_pk_add_f32 v[114:115], v[114:115], 1.0 op_sel_hi:[1,0]
	s_waitcnt vmcnt(10)
	v_pk_add_f32 v[120:121], v[120:121], 1.0 op_sel_hi:[1,0]
	v_pk_add_f32 v[118:119], v[118:119], 1.0 op_sel_hi:[1,0]
	v_pk_mul_f32 v[32:33], v[44:45], v[32:33]
	v_pk_mul_f32 v[30:31], v[42:43], v[30:31]
	v_pk_mul_f32 v[36:37], v[48:49], v[36:37]
	v_pk_mul_f32 v[34:35], v[46:47], v[34:35]
	s_waitcnt vmcnt(9)
	v_pk_mul_f32 v[44:45], v[124:125], v[116:117]
	v_pk_mul_f32 v[42:43], v[122:123], v[114:115]
	s_waitcnt vmcnt(8)
	v_pk_mul_f32 v[48:49], v[128:129], v[120:121]
	v_pk_mul_f32 v[46:47], v[126:127], v[118:119]
	s_waitcnt vmcnt(0)
	s_branch .LBB0_1779

; __device__ __forceinline__ void load_rowvec(RowVec& V, const float* gain, const float* sh, const float* sc, const float* g2, int lane) {
; #pragma unroll
;     for (int j = 0; j < 4; ++j) { const int c = 256 * j + 4 * lane;
;         const f32x4 g = *(const f32x4*)(gain + c), s1 = *(const f32x4*)(sc + c); V.a[j] = g * (s1 + 1.f); V.b[j] = *(const f32x4*)(sh + c);
;         V.g[j] = g2 ? *(const f32x4*)(g2 + c) * MOE_ALPHA : (f32x4){0.f, 0.f, 0.f, 0.f}; }
; }
; __device__ __forceinline__ void mix_norm_phase(Frame& F, int l) {
;     ...
;         const int v = row_class(m);
;         if (v != vcur) { vcur = v; const float* mv = mod + (size_t)(l * 3 + v) * 6144;
;             load_rowvec(V, gain, mv, mv + 1024, l > 0 ? mod + ((size_t)((l - 1) * 3 + v) * 6 + 5) * 1024 : nullptr, F.lane); }
.LBB0_3211:
	s_cmpk_lt_u32 s6, 0x8000
	s_cselect_b32 s15, 1, 2
	s_cmpk_gt_i32 s6, 0x3fff
	s_cselect_b32 s6, s15, 0
	s_cmp_eq_u32 s6, s14
	s_cbranch_scc1 .LBB0_3208
	s_mul_i32 s14, s6, 0x6000
	s_add_u32 s18, s1, s14
	s_addc_u32 s19, s10, 0
	s_add_u32 s14, s18, 0x24000
	s_addc_u32 s15, s19, 0
	s_add_u32 s16, s18, 0x25000
	s_addc_u32 s17, s19, 0
	global_load_dwordx4 v[30:33], v110, s[16:17]
	global_load_dwordx4 v[34:37], v111, s[16:17]
	global_load_dwordx4 v[42:45], v[52:53], off
	global_load_dwordx4 v[46:49], v[54:55], off
	global_load_dwordx4 v[114:117], v112, s[16:17]
	global_load_dwordx4 v[118:121], v113, s[16:17]
	global_load_dwordx4 v[122:125], v[56:57], off
	global_load_dwordx4 v[126:129], v[58:59], off
	s_add_u32 s16, s18, 0x17000
	s_addc_u32 s17, s19, 0
	global_load_dwordx4 v[2:5], v110, s[14:15]
	global_load_dwordx4 v[6:9], v112, s[14:15]
	global_load_dwordx4 v[14:17], v110, s[16:17]
	global_load_dwordx4 v[10:13], v111, s[14:15]
	global_load_dwordx4 v[18:21], v111, s[16:17]
	global_load_dwordx4 v[22:25], v112, s[16:17]
	global_load_dwordx4 v[26:29], v113, s[14:15]
	global_load_dwordx4 v[38:41], v113, s[16:17]
	s_mov_b32 s14, s6
	s_waitcnt vmcnt(15)
	v_pk_add_f32 v[32:33], v[32:33], 1.0 op_sel_hi:[1,0]
	v_pk_add_f32 v[30:31], v[30:31], 1.0 op_sel_hi:[1,0]
	s_waitcnt vmcnt(14)
	v_pk_add_f32 v[36:37], v[36:37], 1.0 op_sel_hi:[1,0]
	v_pk_add_f32 v[34:35], v[34:35], 1.0 op_sel_hi:[1,0]
	s_waitcnt vmcnt(11)
	v_pk_add_f32 v[116:117], v[116:117], 1.0 op_sel_hi:[1,0]
	v_pk_add_f32 v[114:115], v[114:115], 1.0 op_sel_hi:[1,0]
	s_waitcnt vmcnt(10)
	v_pk_add_f32 v[120:121], v[120:121], 1.0 op_sel_hi:[1,0]
	v_pk_add_f32 v[118:119], v[118:119], 1.0 op_sel_hi:[1,0]
	v_pk_mul_f32 v[32:33], v[44:45], v[32:33]
	v_pk_mul_f32 v[30:31], v[42:43], v[30:31]
	v_pk_mul_f32 v[36:37], v[48:49], v[36:37]
	v_pk_mul_f32 v[34:35], v[46:47], v[34:35]
	s_waitcnt vmcnt(9)
	v_pk_mul_f32 v[44:45], v[124:125], v[116:117]
	v_pk_mul_f32 v[42:43], v[122:123], v[114:115]
	s_waitcnt vmcnt(8)
	v_pk_mul_f32 v[48:49], v[128:129], v[120:121]
	v_pk_mul_f32 v[46:47], v[126:127], v[118:119]
	s_waitcnt vmcnt(0)
	s_branch .LBB0_3208

; __device__ __forceinline__ void load_rowvec(RowVec& V, const float* gain, const float* sh, const float* sc, const float* g2, int lane) {
; #pragma unroll
;     for (int j = 0; j < 4; ++j) { const int c = 256 * j + 4 * lane;
;         const f32x4 g = *(const f32x4*)(gain + c), s1 = *(const f32x4*)(sc + c); V.a[j] = g * (s1 + 1.f); V.b[j] = *(const f32x4*)(sh + c);
;         V.g[j] = g2 ? *(const f32x4*)(g2 + c) * MOE_ALPHA : (f32x4){0.f, 0.f, 0.f, 0.f}; }
; }
; __device__ __forceinline__ void mix_norm_phase(Frame& F, int l) {
;     ...
;         const int v = row_class(m);
;         if (v != vcur) { vcur = v; const float* mv = mod + (size_t)(l * 3 + v) * 6144;
;             load_rowvec(V, gain, mv, mv + 1024, l > 0 ? mod + ((size_t)((l - 1) * 3 + v) * 6 + 5) * 1024 : nullptr, F.lane); }
.LBB0_4809:
	s_cmpk_lt_u32 s6, 0x8000
	s_cselect_b32 s15, 1, 2
	s_cmpk_gt_i32 s6, 0x3fff
	s_cselect_b32 s6, s15, 0
	s_cmp_eq_u32 s6, s14
	s_cbranch_scc1 .LBB0_4806
	s_mul_i32 s14, s6, 0x6000
	s_add_u32 s18, s1, s14
	s_addc_u32 s19, s10, 0
	s_add_u32 s14, s18, 0x36000
	s_addc_u32 s15, s19, 0
	s_add_u32 s16, s18, 0x37000
	s_addc_u32 s17, s19, 0
	global_load_dwordx4 v[30:33], v110, s[16:17]
	global_load_dwordx4 v[34:37], v111, s[16:17]
	global_load_dwordx4 v[42:45], v[52:53], off
	global_load_dwordx4 v[46:49], v[54:55], off
	global_load_dwordx4 v[114:117], v112, s[16:17]
	global_load_dwordx4 v[118:121], v113, s[16:17]
	global_load_dwordx4 v[122:125], v[56:57], off
	global_load_dwordx4 v[126:129], v[58:59], off
	s_add_u32 s16, s18, 0x29000
	s_addc_u32 s17, s19, 0
	global_load_dwordx4 v[2:5], v110, s[14:15]
	global_load_dwordx4 v[6:9], v112, s[14:15]
	global_load_dwordx4 v[14:17], v110, s[16:17]
	global_load_dwordx4 v[10:13], v111, s[14:15]
	global_load_dwordx4 v[18:21], v111, s[16:17]
	global_load_dwordx4 v[22:25], v112, s[16:17]
	global_load_dwordx4 v[26:29], v113, s[14:15]
	global_load_dwordx4 v[38:41], v113, s[16:17]
	s_mov_b32 s14, s6
	s_waitcnt vmcnt(15)
	v_pk_add_f32 v[32:33], v[32:33], 1.0 op_sel_hi:[1,0]
	v_pk_add_f32 v[30:31], v[30:31], 1.0 op_sel_hi:[1,0]
	s_waitcnt vmcnt(14)
	v_pk_add_f32 v[36:37], v[36:37], 1.0 op_sel_hi:[1,0]
	v_pk_add_f32 v[34:35], v[34:35], 1.0 op_sel_hi:[1,0]
	s_waitcnt vmcnt(11)
	v_pk_add_f32 v[116:117], v[116:117], 1.0 op_sel_hi:[1,0]
	v_pk_add_f32 v[114:115], v[114:115], 1.0 op_sel_hi:[1,0]
	s_waitcnt vmcnt(10)
	v_pk_add_f32 v[120:121], v[120:121], 1.0 op_sel_hi:[1,0]
	v_pk_add_f32 v[118:119], v[118:119], 1.0 op_sel_hi:[1,0]
	v_pk_mul_f32 v[32:33], v[44:45], v[32:33]
	v_pk_mul_f32 v[30:31], v[42:43], v[30:31]
	v_pk_mul_f32 v[36:37], v[48:49], v[36:37]
	v_pk_mul_f32 v[34:35], v[46:47], v[34:35]
	s_waitcnt vmcnt(9)
	v_pk_mul_f32 v[44:45], v[124:125], v[116:117]
	v_pk_mul_f32 v[42:43], v[122:123], v[114:115]
	s_waitcnt vmcnt(8)
	v_pk_mul_f32 v[48:49], v[128:129], v[120:121]
	v_pk_mul_f32 v[46:47], v[126:127], v[118:119]
	s_waitcnt vmcnt(0)
	s_branch .LBB0_4806
